# speedup vs baseline: 1.0074x; 1.0074x over previous
.Lk2_noprio:
.Lk2_loop:
	s_and_b32 s23, s27, s31
	s_add_u32 s24, s20, s23
	s_addc_u32 s25, s21, 0
	s_add_u32 s27, s27, s28
	s_waitcnt vmcnt(7)
	s_waitcnt lgkmcnt(2)
	v_mfma_f32_32x32x16_f16 a[0:15], v[64:67], v[128:131], a[0:15]
	v_pk_max_u16 v132, v148, v42
	v_pk_max_u16 v133, v149, v42
	v_pk_max_u16 v134, v150, v42
	v_pk_max_u16 v135, v151, v42
	v_mfma_f32_32x32x16_f16 a[16:31], v[64:67], v[136:139], a[16:31]
	v_pk_max_u16 v140, v148, v43
	v_pk_max_u16 v141, v149, v43
	v_pk_max_u16 v142, v150, v43
	v_pk_max_u16 v143, v151, v43
	v_mfma_f32_16x16x32_f16 a[32:35], v[160:163], v[128:131], a[32:35]
	global_load_dwordx4 v[64:67], v1, s[24:25]
	ds_read_b128 v[156:159], v46 offset:96
	ds_read_b128 v[168:171], v47 offset:64
	v_mfma_f32_16x16x32_f16 a[36:39], v[160:163], v[136:139], a[36:39]
	s_and_b32 s23, s27, s31
	s_add_u32 s24, s20, s23
	s_addc_u32 s25, s21, 0
	s_add_u32 s27, s27, s28
	s_waitcnt vmcnt(7)
	s_waitcnt lgkmcnt(2)
	v_mfma_f32_32x32x16_f16 a[0:15], v[68:71], v[132:135], a[0:15]
	v_pk_max_u16 v128, v152, v42
	v_pk_max_u16 v129, v153, v42
	v_pk_max_u16 v130, v154, v42
	v_pk_max_u16 v131, v155, v42
	v_mfma_f32_32x32x16_f16 a[16:31], v[68:71], v[140:143], a[16:31]
	v_pk_max_u16 v136, v152, v43
	v_pk_max_u16 v137, v153, v43
	v_pk_max_u16 v138, v154, v43
	v_pk_max_u16 v139, v155, v43
	v_mfma_f32_16x16x32_f16 a[32:35], v[164:167], v[132:135], a[32:35]
	global_load_dwordx4 v[68:71], v1, s[24:25]
	ds_read_b128 v[144:147], v46 offset:128
	ds_read_b128 v[172:175], v47 offset:96
	v_mfma_f32_16x16x32_f16 a[36:39], v[164:167], v[140:143], a[36:39]
	s_and_b32 s23, s27, s31
	s_add_u32 s24, s20, s23
	s_addc_u32 s25, s21, 0
	s_add_u32 s27, s27, s28
	s_waitcnt vmcnt(7)
	s_waitcnt lgkmcnt(2)
	v_mfma_f32_32x32x16_f16 a[0:15], v[72:75], v[128:131], a[0:15]
	v_pk_max_u16 v132, v156, v42
	v_pk_max_u16 v133, v157, v42
	v_pk_max_u16 v134, v158, v42
	v_pk_max_u16 v135, v159, v42
	v_mfma_f32_32x32x16_f16 a[16:31], v[72:75], v[136:139], a[16:31]
	v_pk_max_u16 v140, v156, v43
	v_pk_max_u16 v141, v157, v43
	v_pk_max_u16 v142, v158, v43
	v_pk_max_u16 v143, v159, v43
	v_mfma_f32_16x16x32_f16 a[32:35], v[168:171], v[128:131], a[32:35]
	global_load_dwordx4 v[72:75], v1, s[24:25]
	ds_read_b128 v[148:151], v46 offset:160
	ds_read_b128 v[160:163], v47 offset:128
	v_mfma_f32_16x16x32_f16 a[36:39], v[168:171], v[136:139], a[36:39]
	s_and_b32 s23, s27, s31
	s_add_u32 s24, s20, s23
	s_addc_u32 s25, s21, 0
	s_add_u32 s27, s27, s28
	s_waitcnt vmcnt(7)
	s_waitcnt lgkmcnt(2)
	v_mfma_f32_32x32x16_f16 a[0:15], v[76:79], v[132:135], a[0:15]
	v_pk_max_u16 v128, v144, v42
	v_pk_max_u16 v129, v145, v42
	v_pk_max_u16 v130, v146, v42
	v_pk_max_u16 v131, v147, v42
	v_mfma_f32_32x32x16_f16 a[16:31], v[76:79], v[140:143], a[16:31]
	v_pk_max_u16 v136, v144, v43
	v_pk_max_u16 v137, v145, v43
	v_pk_max_u16 v138, v146, v43
	v_pk_max_u16 v139, v147, v43
	v_mfma_f32_16x16x32_f16 a[32:35], v[172:175], v[132:135], a[32:35]
	global_load_dwordx4 v[76:79], v1, s[24:25]
	ds_read_b128 v[152:155], v46 offset:192
	ds_read_b128 v[164:167], v47 offset:160
	v_mfma_f32_16x16x32_f16 a[36:39], v[172:175], v[140:143], a[36:39]
	s_and_b32 s23, s27, s31
	s_add_u32 s24, s20, s23
	s_addc_u32 s25, s21, 0
	s_add_u32 s27, s27, s28
	s_waitcnt vmcnt(7)
	s_waitcnt lgkmcnt(2)
	v_mfma_f32_32x32x16_f16 a[0:15], v[80:83], v[128:131], a[0:15]
	v_pk_max_u16 v132, v148, v42
	v_pk_max_u16 v133, v149, v42
	v_pk_max_u16 v134, v150, v42
	v_pk_max_u16 v135, v151, v42
	v_mfma_f32_32x32x16_f16 a[16:31], v[80:83], v[136:139], a[16:31]
	v_pk_max_u16 v140, v148, v43
	v_pk_max_u16 v141, v149, v43
	v_pk_max_u16 v142, v150, v43
	v_pk_max_u16 v143, v151, v43
	v_mfma_f32_16x16x32_f16 a[32:35], v[160:163], v[128:131], a[32:35]
	global_load_dwordx4 v[80:83], v1, s[24:25]
	ds_read_b128 v[156:159], v46 offset:224
	ds_read_b128 v[168:171], v47 offset:192
	v_mfma_f32_16x16x32_f16 a[36:39], v[160:163], v[136:139], a[36:39]
	s_and_b32 s23, s27, s31
	s_add_u32 s24, s20, s23
	s_addc_u32 s25, s21, 0
	s_add_u32 s27, s27, s28
	s_waitcnt vmcnt(7)
	s_waitcnt lgkmcnt(2)
	v_mfma_f32_32x32x16_f16 a[0:15], v[84:87], v[132:135], a[0:15]
	v_pk_max_u16 v128, v152, v42
	v_pk_max_u16 v129, v153, v42
	v_pk_max_u16 v130, v154, v42
	v_pk_max_u16 v131, v155, v42
	v_mfma_f32_32x32x16_f16 a[16:31], v[84:87], v[140:143], a[16:31]
	v_pk_max_u16 v136, v152, v43
	v_pk_max_u16 v137, v153, v43
	v_pk_max_u16 v138, v154, v43
	v_pk_max_u16 v139, v155, v43
	v_mfma_f32_16x16x32_f16 a[32:35], v[164:167], v[132:135], a[32:35]
	global_load_dwordx4 v[84:87], v1, s[24:25]
	ds_read_b128 v[144:147], v46 offset:256
	ds_read_b128 v[172:175], v47 offset:224
	v_mfma_f32_16x16x32_f16 a[36:39], v[164:167], v[140:143], a[36:39]
	s_and_b32 s23, s27, s31
	s_add_u32 s24, s20, s23
	s_addc_u32 s25, s21, 0
	s_add_u32 s27, s27, s28
	s_waitcnt vmcnt(7)
	s_waitcnt lgkmcnt(2)
	v_mfma_f32_32x32x16_f16 a[0:15], v[88:91], v[128:131], a[0:15]
	v_pk_max_u16 v132, v156, v42
	v_pk_max_u16 v133, v157, v42
	v_pk_max_u16 v134, v158, v42
	v_pk_max_u16 v135, v159, v42
	v_mfma_f32_32x32x16_f16 a[16:31], v[88:91], v[136:139], a[16:31]
	v_pk_max_u16 v140, v156, v43
	v_pk_max_u16 v141, v157, v43
	v_pk_max_u16 v142, v158, v43
	v_pk_max_u16 v143, v159, v43
	v_mfma_f32_16x16x32_f16 a[32:35], v[168:171], v[128:131], a[32:35]
	global_load_dwordx4 v[88:91], v1, s[24:25]
	ds_read_b128 v[148:151], v46 offset:288
	ds_read_b128 v[160:163], v47 offset:256
	v_mfma_f32_16x16x32_f16 a[36:39], v[168:171], v[136:139], a[36:39]
	s_and_b32 s23, s27, s31
	s_add_u32 s24, s20, s23
	s_addc_u32 s25, s21, 0
	s_add_u32 s27, s27, s28
	s_waitcnt vmcnt(7)
	s_waitcnt lgkmcnt(2)
	v_mfma_f32_32x32x16_f16 a[0:15], v[92:95], v[132:135], a[0:15]
	v_pk_max_u16 v128, v144, v42
	v_pk_max_u16 v129, v145, v42
	v_pk_max_u16 v130, v146, v42
	v_pk_max_u16 v131, v147, v42
	v_mfma_f32_32x32x16_f16 a[16:31], v[92:95], v[140:143], a[16:31]
	v_pk_max_u16 v136, v144, v43
	v_pk_max_u16 v137, v145, v43
	v_pk_max_u16 v138, v146, v43
	v_pk_max_u16 v139, v147, v43
	v_mfma_f32_16x16x32_f16 a[32:35], v[172:175], v[132:135], a[32:35]
	global_load_dwordx4 v[92:95], v1, s[24:25]
	ds_read_b128 v[152:155], v46 offset:320
	ds_read_b128 v[164:167], v47 offset:288
	v_add_u32_e32 v46, 256, v46
	v_add_u32_e32 v47, 256, v47
	v_mfma_f32_16x16x32_f16 a[36:39], v[172:175], v[140:143], a[36:39]
	s_add_u32 s26, s26, 1
	s_cmp_lt_u32 s26, 7
	s_cbranch_scc1 .Lk2_loop
	s_cmp_lt_u32 s26, 8
	s_cbranch_scc0 .Lk2_loopdone
	s_mov_b32 s27, s29
	s_mov_b32 s28, 0
	s_branch .Lk2_loop
.Lk2_loopdone:
	v_and_b32_e32 v2, 63, v0
	v_lshrrev_b32_e32 v3, 5, v2
	v_and_b32_e32 v4, 31, v0
	s_lshl_b32 s23, s15, 4
	v_add_u32_e32 v3, s23, v3
	v_mul_u32_u24_e32 v3, 576, v3
	v_lshl_add_u32 v3, v4, 4, v3
	v_cmp_gt_u32_e32 vcc, 16, v2
	ds_write_b128 v3, a[0:3]
	ds_write_b128 v3, a[16:19] offset:4608
	ds_write_b128 v3, a[4:7] offset:1152
	ds_write_b128 v3, a[20:23] offset:5760
	ds_write_b128 v3, a[8:11] offset:2304
	ds_write_b128 v3, a[24:27] offset:6912
	ds_write_b128 v3, a[12:15] offset:3456
	ds_write_b128 v3, a[28:31] offset:8064
	s_and_saveexec_b64 s[2:3], vcc
	s_cbranch_execz .Lk2_nodred
	v_lshlrev_b32_e32 v5, 2, v2
	s_lshl_b32 s23, s15, 8
	v_add_u32_e32 v5, s23, v5
	v_add_u32_e32 v5, 73728, v5
	ds_write2_b32 v5, a32, a33 offset1:16
	ds_write2_b32 v5, a36, a37 offset0:32 offset1:48
